# t1: br1 + first attention pass requests K/V tile 1 together with tile 0 (before the tile-0 wait)
# baseline (speedup 1.0000x reference)
; __device__ __forceinline__ int v_st(int k, int c) { const int kk = (k & ~0xC) | ((k & 4) << 1) | ((k & 8) >> 1); return ((kk >> 3) * 4 + (c >> 5)) * 512 + ((kk & 7) * 32 + (c & 31)) * 2; }
; __device__ __forceinline__ int v_rd_base(int lane) { return ((lane & 3) << 3) | (((lane >> 2) & 3) << 6) | (((lane >> 4) & 1) << 5) | (((lane >> 5) & 1) << 8); }
; #define SLOAD(k0) do { vs0 = *reinterpret_cast<const bf16x8*>(&Vh[(size_t)((k0) + sr) * DM + sc]); vs1 = *reinterpret_cast<const bf16x8*>(&Vh[(size_t)((k0) + 32 + sr) * DM + sc]); \
;     ks = *reinterpret_cast<const bf16x8*>(&Kh[(size_t)((k0) + kr) * DM + kc]); } while (0)
; #define SWRITE(s) do { *(bf16x8*)(V_lds + (s) * SHM_V + vst0) = vs0; *(bf16x8*)(V_lds + (s) * SHM_V + vst1) = vs1; *(bf16x8*)(K_lds + (s) * SHM_K64 + kst) = ks; } while (0)
; __device__ __forceinline__ void diff_pass(const bf16_t* __restrict__ Qb, const bf16_t* __restrict__ Kh, const bf16_t* __restrict__ Vh, int seq, char* lds, f32x16 (&o)[4], const int wave_) {
;     ...
;     const bf16_t* Qw = Qb + (size_t)(wid * 32 + r32) * DM + hi * 8;
; #pragma unroll
;     for (int d0 = 0; d0 < 4; ++d0) qr[d0] = *reinterpret_cast<const bf16x8*>(Qw + d0 * 16);
;     const int sr = tid >> 4, sc = (tid & 15) * 8, vst0 = v_st(sr, sc), vst1 = v_st(32 + sr, sc);
;     const int kr = tid >> 3, kc = (tid & 7) * 8, kst = kswz<64>(kr, kc * 2);
;     const int vb0 = (int)(uintptr_t)V_lds + v_rd_base(lane);
;     bf16x8 vs0, vs1, ks;
;     ...
;     __syncthreads();
;     SLOAD(0); SWRITE(0); SLOAD(64); __syncthreads();
.LBB0_822:
	s_lshl_b32 s0, s36, 1
	s_mov_b32 s1, -1
	s_and_b32 s64, s0, 0x700
	s_ashr_i32 s0, s37, 6
	s_lshl_b32 s2, s37, 8
	v_mbcnt_lo_u32_b32 v0, s1, 0
	v_mbcnt_hi_u32_b32 v0, s1, v0
	s_ashr_i32 s1, s0, 31
	s_lshl_b64 s[6:7], s[0:1], 11
	s_and_b32 s2, s2, 0x700
	s_or_b32 s6, s6, s2
	s_lshl_b64 s[2:3], s[6:7], 11
	v_readlane_b32 s8, v252, 16
	v_readlane_b32 s9, v252, 17
	s_add_u32 s2, s8, s2
	s_addc_u32 s3, s9, s3
	s_lshl_b32 s8, s37, 4
	s_and_b32 s38, s8, 0x380
	s_lshl_b32 s8, s38, 1
	s_add_u32 s34, s2, s8
	s_addc_u32 s35, s3, 0
	s_lshl_b64 s[10:11], s[0:1], 22
	v_readlane_b32 s0, v251, 42
	s_add_u32 s0, s0, s10
	v_readlane_b32 s1, v251, 43
	s_addc_u32 s1, s1, s11
	s_add_u32 s28, s0, s8
	s_addc_u32 s29, s1, 0
	v_readlane_b32 s0, v251, 44
	s_add_u32 s0, s0, s10
	v_readlane_b32 s1, v251, 45
	s_addc_u32 s1, s1, s11
	v_or_b32_e32 v207, s55, v0
	s_add_u32 s30, s0, s8
	s_mov_b32 s0, -1
	s_addc_u32 s31, s1, 0
	v_mbcnt_lo_u32_b32 v0, s0, 0
	v_mbcnt_hi_u32_b32 v0, s0, v0
	v_or_b32_e32 v68, s55, v0
	s_movk_i32 s0, 0xffe0
	v_ashrrev_i32_e32 v0, 1, v68
	v_bfi_b32 v0, s0, v0, v68
	v_ashrrev_i32_e32 v1, 31, v0
	v_lshlrev_b64 v[0:1], 11, v[0:1]
	v_lshrrev_b32_e32 v2, 1, v68
	v_ashrrev_i32_e32 v12, 4, v68
	v_lshl_add_u64 v[0:1], s[34:35], 0, v[0:1]
	v_and_b32_e32 v160, 16, v2
	v_lshlrev_b32_e32 v24, 3, v68
	v_ashrrev_i32_e32 v13, 31, v12
	v_lshl_add_u64 v[0:1], v[0:1], 0, v[160:161]
	v_and_b32_e32 v2, 0x78, v24
	v_lshlrev_b64 v[48:49], 11, v[12:13]
	global_load_dwordx4 v[162:165], v[0:1], off
	global_load_dwordx4 v[166:169], v[0:1], off offset:32
	global_load_dwordx4 v[170:173], v[0:1], off offset:64
	global_load_dwordx4 v[174:177], v[0:1], off offset:96
	v_lshl_add_u64 v[0:1], s[30:31], 0, v[48:49]
	v_lshlrev_b32_e32 v4, 1, v2
	v_mov_b32_e32 v5, v161
	v_add_u32_e32 v14, 32, v12
	v_ashrrev_i32_e32 v16, 3, v68
	v_lshl_add_u64 v[18:19], v[0:1], 0, v[4:5]
	s_barrier
	global_load_dwordx4 v[0:3], v[18:19], off
	v_ashrrev_i32_e32 v15, 31, v14
	v_ashrrev_i32_e32 v17, 31, v16
	v_lshlrev_b32_e32 v64, 4, v68
	v_lshlrev_b64 v[6:7], 11, v[14:15]
	v_lshlrev_b64 v[50:51], 11, v[16:17]
	v_lshl_add_u64 v[6:7], s[30:31], 0, v[6:7]
	v_and_b32_e32 v20, 0x70, v64
	v_lshl_add_u64 v[8:9], s[28:29], 0, v[50:51]
	v_mov_b32_e32 v21, v161
	v_lshl_add_u64 v[4:5], v[6:7], 0, v[4:5]
	v_lshl_add_u64 v[22:23], v[8:9], 0, v[20:21]
	global_load_dwordx4 v[4:7], v[4:5], off
	v_and_b32_e32 v13, 0xfffff0, v12
	global_load_dwordx4 v[8:11], v[22:23], off
	v_add_co_u32_e32 v194, vcc, 0x20000, v18
	s_nop 1
	v_addc_co_u32_e32 v195, vcc, 0, v19, vcc
	global_load_dwordx4 v[52:55], v[194:195], off
	v_add_co_u32_e32 v194, vcc, 0x30000, v18
	s_nop 1
	v_addc_co_u32_e32 v195, vcc, 0, v19, vcc
	global_load_dwordx4 v[56:59], v[194:195], off
	v_add_co_u32_e32 v194, vcc, 0x20000, v22
	s_nop 1
	v_addc_co_u32_e32 v195, vcc, 0, v23, vcc
	global_load_dwordx4 v[60:63], v[194:195], off
	v_lshlrev_b32_e32 v15, 1, v12
	v_and_or_b32 v13, v15, 8, v13
	v_lshrrev_b32_e32 v15, 1, v12
	v_lshrrev_b32_e32 v13, 1, v13
	v_bfe_u32 v17, v24, 5, 2
	v_and_b32_e32 v12, 3, v12
	v_or_b32_e32 v13, v13, v17
	v_and_or_b32 v12, v15, 4, v12
	v_lshlrev_b32_e32 v13, 9, v13
	v_lshlrev_b32_e32 v12, 6, v12
	v_and_b32_e32 v15, 48, v64
	v_or3_b32 v218, v13, v12, v15
	v_and_b32_e32 v13, 0xfffff0, v14
	v_lshlrev_b32_e32 v14, 1, v14
	v_and_or_b32 v13, v14, 8, v13
	v_lshrrev_b32_e32 v13, 1, v13
	v_or_b32_e32 v13, v13, v17
	v_add_u32_e32 v70, 0, v218
	s_mov_b32 s0, 0x20000
	v_lshlrev_b32_e32 v13, 9, v13
	v_or3_b32 v219, v13, v12, v15
	v_lshlrev_b32_e32 v12, 7, v16
	v_and_b32_e32 v13, 0x70, v68
	s_mov_b32 s1, 0x30000
	v_bitop3_b32 v220, v20, v12, v13 bitop3:0xde
	v_add_u32_e32 v71, 0, v219
	v_add_u32_e32 v221, 0, v220
	v_and_b32_e32 v69, 31, v68
	v_lshlrev_b32_e32 v12, 7, v69
	v_and_b32_e32 v13, 0x70, v24
	v_bitop3_b32 v223, v160, v12, v13 bitop3:0xde
	v_add_u32_e32 v222, 0, v223
	s_add_i32 s39, 0, 0x12000
	v_and_b32_e32 v72, 63, v68
	s_mov_b32 s12, 0
	s_mov_b32 s13, s12
	s_mov_b32 s14, s12
	s_mov_b32 s15, s12
	s_mov_b32 s16, s12
	s_mov_b32 s17, s12
	s_mov_b32 s18, s12
	s_mov_b32 s19, s12
	s_mov_b32 s20, s12
	s_mov_b32 s21, s12
	s_mov_b32 s22, s12
	s_mov_b32 s23, s12
	s_mov_b32 s24, s12
	s_mov_b32 s25, s12
	s_mov_b32 s26, s12
	s_mov_b32 s27, s12
	s_cmp_lg_u32 0, -1
	s_mov_b32 s42, 1
	s_mov_b32 s40, -1
	s_mov_b32 s41, 2
	v_mov_b32_e32 v230, 1.0
	v_mov_b32_e32 v215, 0
	s_waitcnt vmcnt(5)
	ds_write_b128 v70, v[0:3]
	s_waitcnt vmcnt(4)
	ds_write_b128 v71, v[4:7]
	s_waitcnt vmcnt(3)
	ds_write_b128 v221, v[8:11] offset:49152
	v_and_b32_e32 v8, 0x3fffffc0, v68
	s_waitcnt lgkmcnt(0)
	s_barrier
; #define SWRITE(s) do { *(bf16x8*)(V_lds + (s) * SHM_V + vst0) = vs0; *(bf16x8*)(V_lds + (s) * SHM_V + vst1) = vs1; *(bf16x8*)(K_lds + (s) * SHM_K64 + kst) = ks; } while (0)
; #define EX2(x) x = __builtin_amdgcn_exp2f(x)
; __device__ __forceinline__ void diff_pass(const bf16_t* __restrict__ Qb, const bf16_t* __restrict__ Kh, const bf16_t* __restrict__ Vh, int seq, char* lds, f32x16 (&o)[4], const int wave_) {
;     ...
;     negm = f32x16{};
;     qkt64c(pA0, pA1, K_lds, qr, negm, r32, hi);
;     { const float pm = rowmax32(pA0, pA1); m_reg = pm; alA = 1.f;
; #pragma unroll
;       for (int r = 0; r < 16; ++r) { pA0[r] -= pm; pA1[r] -= pm; negm[r] = -pm; }
; #pragma unroll
;       for (int r = 0; r < 16; ++r) EX2(pA0[r]);
; #pragma unroll
;       for (int r = 0; r < 8; ++r) EX2(pA1[r]); }
;     SWRITE(1); __syncthreads();
	ds_read_b128 v[0:3], v222 offset:49152
	ds_read_b128 v[4:7], v222 offset:53248
	s_waitcnt lgkmcnt(1)
	v_mfma_f32_32x32x16_bf16 v[16:31], v[0:3], v[162:165], 0
	v_or_b32_e32 v0, 32, v160
	v_bitop3_b32 v226, v0, v12, v13 bitop3:0xde
	v_add_u32_e32 v224, 0, v226
	ds_read_b128 v[0:3], v224 offset:49152
	v_lshl_add_u32 v213, v8, 2, s39
	s_cselect_b32 s0, 0, 0
	v_lshl_add_u32 v214, v69, 2, v213
	s_waitcnt lgkmcnt(1)
	v_mfma_f32_32x32x16_bf16 v[32:47], v[4:7], v[162:165], 0
	ds_read_b128 v[4:7], v224 offset:53248
	s_waitcnt lgkmcnt(1)
	v_mfma_f32_32x32x16_bf16 v[16:31], v[0:3], v[166:169], v[16:31]
	v_or_b32_e32 v0, 64, v160
	v_bitop3_b32 v228, v0, v12, v13 bitop3:0xde
	v_add_u32_e32 v225, 0, v228
	ds_read_b128 v[0:3], v225 offset:53248
	ds_read_b128 v[8:11], v225 offset:49152
	s_waitcnt lgkmcnt(2)
	v_mfma_f32_32x32x16_bf16 v[32:47], v[4:7], v[166:169], v[32:47]
	v_lshlrev_b32_e32 v4, 3, v72
	v_and_b32_e32 v5, 0xc0, v64
	v_lshlrev_b32_e32 v6, 1, v68
	v_and_or_b32 v5, v4, 24, v5
	v_and_b32_e32 v6, 32, v6
	v_and_b32_e32 v4, 0x100, v4
	v_or3_b32 v216, v5, v6, v4
	s_waitcnt lgkmcnt(0)
	v_mfma_f32_32x32x16_bf16 v[16:31], v[8:11], v[170:173], v[16:31]
	v_or_b32_e32 v4, 0x60, v160
	v_bitop3_b32 v229, v4, v12, v13 bitop3:0xde
	v_add_u32_e32 v227, 0, v229
	ds_read_b128 v[64:67], v227 offset:53248
	ds_read_b128 v[4:7], v227 offset:49152
	s_waitcnt vmcnt(2)
	ds_write_b128 v70, v[52:55] offset:16384
	s_waitcnt vmcnt(1)
	ds_write_b128 v71, v[56:59] offset:16384
	s_waitcnt vmcnt(0)
	ds_write_b128 v221, v[60:63] offset:57344
	v_mfma_f32_32x32x16_bf16 v[32:47], v[0:3], v[170:173], v[32:47]
	v_add_u32_e32 v217, s0, v216
	v_cmp_gt_u32_e64 s[0:1], 32, v72
	s_waitcnt lgkmcnt(0)
	s_barrier
	v_mfma_f32_32x32x16_bf16 v[16:31], v[4:7], v[174:177], v[16:31]
	v_mov_b64_e32 v[0:1], s[12:13]
	v_mov_b64_e32 v[14:15], s[26:27]
	v_mov_b64_e32 v[2:3], s[14:15]
	v_mov_b64_e32 v[4:5], s[16:17]
	v_mov_b64_e32 v[6:7], s[18:19]
	v_mov_b64_e32 v[8:9], s[20:21]
	v_mov_b64_e32 v[10:11], s[22:23]
	v_mfma_f32_32x32x16_bf16 v[32:47], v[64:67], v[174:177], v[32:47]
	s_nop 3
	v_max_f32_e32 v64, v17, v17
	v_max_f32_e32 v65, v16, v16
	v_max_f32_e32 v64, v65, v64
	v_mov_b64_e32 v[12:13], s[24:25]
	s_nop 3
	v_max3_f32 v65, v18, v19, v33
	v_max3_f32 v64, v64, v32, v34
	v_max3_f32 v64, v64, v35, v20
	v_max3_f32 v65, v65, v22, v23
	v_max3_f32 v64, v64, v21, v36
	v_max3_f32 v65, v65, v38, v39
	v_max3_f32 v64, v64, v37, v24
	v_max3_f32 v65, v65, v26, v27
	v_max3_f32 v64, v64, v25, v40
	v_max3_f32 v65, v65, v42, v43
	v_max3_f32 v64, v64, v41, v28
	v_max3_f32 v65, v65, v30, v31
	v_max3_f32 v64, v64, v29, v44
	v_max3_f32 v65, v65, v46, v47
	v_max3_f32 v64, v64, v45, v65
	v_mov_b32_e32 v65, v64
	s_nop 1
	v_permlane32_swap_b32_e32 v64, v65
	v_max_f32_e32 v65, v65, v65
	v_max_f32_e32 v64, v64, v64
	v_max_f32_e32 v196, v64, v65
	v_sub_f32_e32 v16, v16, v196
	v_sub_f32_e32 v17, v17, v196
	v_sub_f32_e32 v18, v18, v196
	v_exp_f32_e32 v96, v16
	v_exp_f32_e32 v97, v17
	v_exp_f32_e32 v98, v18
	v_lshl_add_u64 v[16:17], s[10:11], 0, v[50:51]
	v_and_b32_e32 v18, 7, v68
	v_sub_f32_e32 v32, v32, v196
	v_sub_f32_e32 v33, v33, v196
	v_sub_f32_e32 v34, v34, v196
	v_sub_f32_e32 v19, v19, v196
	v_sub_f32_e32 v35, v35, v196
	v_sub_f32_e32 v20, v20, v196
	v_sub_f32_e32 v36, v36, v196
	v_sub_f32_e32 v21, v21, v196
	v_sub_f32_e32 v37, v37, v196
	v_sub_f32_e32 v22, v22, v196
	v_sub_f32_e32 v38, v38, v196
	v_sub_f32_e32 v23, v23, v196
	v_sub_f32_e32 v39, v39, v196
	v_sub_f32_e32 v24, v24, v196
	v_sub_f32_e32 v25, v25, v196
	v_sub_f32_e32 v26, v26, v196
	v_sub_f32_e32 v27, v27, v196
	v_sub_f32_e32 v28, v28, v196
	v_sub_f32_e32 v29, v29, v196
	v_sub_f32_e32 v30, v30, v196
	v_sub_f32_e32 v31, v31, v196
	v_lshl_or_b32 v16, v18, 4, v16
	v_exp_f32_e32 v99, v19
	v_exp_f32_e32 v100, v20
	v_exp_f32_e32 v101, v21
	v_exp_f32_e32 v102, v22
	v_exp_f32_e32 v103, v23
	v_exp_f32_e32 v104, v24
	v_exp_f32_e32 v105, v25
	v_exp_f32_e32 v106, v26
	v_exp_f32_e32 v107, v27
	v_exp_f32_e32 v108, v28
	v_exp_f32_e32 v109, v29
	v_exp_f32_e32 v110, v30
	v_exp_f32_e32 v111, v31
	v_exp_f32_e32 v112, v32
	v_exp_f32_e32 v113, v33
	v_exp_f32_e32 v114, v34
	v_exp_f32_e32 v115, v35
	v_exp_f32_e32 v116, v36
	v_exp_f32_e32 v117, v37
	v_exp_f32_e32 v118, v38
	v_exp_f32_e32 v119, v39
	v_lshl_add_u64 v[198:199], s[52:53], 0, v[16:17]
	v_lshl_add_u64 v[16:17], s[10:11], 0, v[48:49]
	v_and_b32_e32 v18, 15, v68
	v_lshl_or_b32 v16, v18, 4, v16
	v_xor_b32_e32 v80, 0x80000000, v196
	v_pk_add_f32 v[120:121], v[40:41], v[196:197] op_sel_hi:[1,0] neg_lo:[0,1] neg_hi:[0,1]
	v_pk_add_f32 v[122:123], v[42:43], v[196:197] op_sel_hi:[1,0] neg_lo:[0,1] neg_hi:[0,1]
	v_pk_add_f32 v[124:125], v[44:45], v[196:197] op_sel_hi:[1,0] neg_lo:[0,1] neg_hi:[0,1]
	v_pk_add_f32 v[126:127], v[46:47], v[196:197] op_sel_hi:[1,0] neg_lo:[0,1] neg_hi:[0,1]
	v_lshl_add_u64 v[200:201], s[52:53], 0, v[16:17]
	v_mov_b64_e32 v[62:63], v[14:15]
	v_mov_b64_e32 v[46:47], v[14:15]
	v_mov_b64_e32 v[30:31], v[14:15]
	v_mov_b64_e32 v[60:61], v[12:13]
	v_mov_b64_e32 v[58:59], v[10:11]
	v_mov_b64_e32 v[56:57], v[8:9]
	v_mov_b64_e32 v[54:55], v[6:7]
	v_mov_b64_e32 v[52:53], v[4:5]
	v_mov_b64_e32 v[50:51], v[2:3]
	v_mov_b64_e32 v[48:49], v[0:1]
	v_mov_b64_e32 v[44:45], v[12:13]
	v_mov_b64_e32 v[42:43], v[10:11]
	v_mov_b64_e32 v[40:41], v[8:9]
	v_mov_b64_e32 v[38:39], v[6:7]
	v_mov_b64_e32 v[36:37], v[4:5]
	v_mov_b64_e32 v[34:35], v[2:3]
	v_mov_b64_e32 v[32:33], v[0:1]
	v_mov_b64_e32 v[28:29], v[12:13]
	v_mov_b64_e32 v[26:27], v[10:11]
	v_mov_b64_e32 v[24:25], v[8:9]
	v_mov_b64_e32 v[22:23], v[6:7]
	v_mov_b64_e32 v[20:21], v[4:5]
	v_mov_b64_e32 v[18:19], v[2:3]
	v_mov_b64_e32 v[16:17], v[0:1]
	v_mov_b32_e32 v81, v80
	v_mov_b32_e32 v82, v80
	v_mov_b32_e32 v83, v80
	v_mov_b32_e32 v84, v80
	v_mov_b32_e32 v85, v80
	v_mov_b32_e32 v86, v80
	v_mov_b32_e32 v87, v80
	v_mov_b32_e32 v88, v80
	v_mov_b32_e32 v89, v80
	v_mov_b32_e32 v90, v80
	v_mov_b32_e32 v91, v80
	v_mov_b32_e32 v92, v80
	v_mov_b32_e32 v93, v80
	v_mov_b32_e32 v94, v80
	v_mov_b32_e32 v95, v80
